# combo12a + nt on the P7 gate-matrix image stores (268 MB streamed)
# baseline (speedup 1.0000x reference)
.LBB0_831:
	s_or_b64 exec, exec, s[4:5]
	v_add_u32_e32 v157, s29, v47
	s_waitcnt lgkmcnt(0)
	s_barrier
	ds_read_b128 v[158:161], v157
	v_add_u32_e32 v162, s6, v149
	v_ashrrev_i32_e32 v163, 31, v162
	v_lshlrev_b64 v[162:163], 16, v[162:163]
	v_lshl_add_u64 v[166:167], v[0:1], 0, v[162:163]
	ds_read_b128 v[162:165], v135
	s_waitcnt lgkmcnt(1)
	global_store_dwordx4 v[166:167], v[158:161], off nt
	s_add_i32 s7, s7, -1
	s_cmp_eq_u32 s7, 0
	v_add_u32_e32 v158, s6, v150
	v_ashrrev_i32_e32 v159, 31, v158
	v_lshlrev_b64 v[158:159], 16, v[158:159]
	v_lshl_add_u64 v[158:159], v[2:3], 0, v[158:159]
	s_waitcnt lgkmcnt(0)
	global_store_dwordx4 v[158:159], v[162:165], off nt
	ds_read_b128 v[158:161], v136
	v_add_u32_e32 v150, 4, v150
	v_add_u32_e32 v162, s6, v151
	v_ashrrev_i32_e32 v163, 31, v162
	v_lshlrev_b64 v[162:163], 16, v[162:163]
	v_lshl_add_u64 v[166:167], v[0:1], 0, v[162:163]
	ds_read_b128 v[162:165], v137
	s_waitcnt lgkmcnt(1)
	global_store_dwordx4 v[166:167], v[158:161], off nt
	v_add_u32_e32 v151, 4, v151
	v_add_u32_e32 v149, 4, v149
	v_add_u32_e32 v158, s6, v152
	v_ashrrev_i32_e32 v159, 31, v158
	v_lshlrev_b64 v[158:159], 16, v[158:159]
	v_lshl_add_u64 v[158:159], v[4:5], 0, v[158:159]
	s_waitcnt lgkmcnt(0)
	global_store_dwordx4 v[158:159], v[162:165], off nt
	ds_read_b128 v[158:161], v138
	v_add_u32_e32 v152, 4, v152
	v_add_u32_e32 v162, s6, v153
	v_ashrrev_i32_e32 v163, 31, v162
	v_lshlrev_b64 v[162:163], 16, v[162:163]
	v_lshl_add_u64 v[166:167], v[0:1], 0, v[162:163]
	ds_read_b128 v[162:165], v139
	s_waitcnt lgkmcnt(1)
	global_store_dwordx4 v[166:167], v[158:161], off nt
	v_add_u32_e32 v153, 4, v153
	ds_write_b128 v157, v[190:193]
	v_add_u32_e32 v158, s6, v154
	v_ashrrev_i32_e32 v159, 31, v158
	v_lshlrev_b64 v[158:159], 16, v[158:159]
	v_lshl_add_u64 v[158:159], v[6:7], 0, v[158:159]
	s_waitcnt lgkmcnt(1)
	global_store_dwordx4 v[158:159], v[162:165], off nt
	ds_read_b128 v[158:161], v140
	v_add_u32_e32 v154, 4, v154
	v_add_u32_e32 v162, s6, v155
	v_ashrrev_i32_e32 v163, 31, v162
	v_lshlrev_b64 v[162:163], 16, v[162:163]
	v_lshl_add_u64 v[166:167], v[0:1], 0, v[162:163]
	ds_read_b128 v[162:165], v141
	s_waitcnt lgkmcnt(1)
	global_store_dwordx4 v[166:167], v[158:161], off nt
	v_add_u32_e32 v155, 4, v155
	ds_write_b128 v135, v[190:193]
	v_add_u32_e32 v158, s6, v156
	v_ashrrev_i32_e32 v159, 31, v158
	v_lshlrev_b64 v[158:159], 16, v[158:159]
	v_lshl_add_u64 v[158:159], v[8:9], 0, v[158:159]
	v_add_u32_e32 v156, 4, v156
	ds_write_b128 v136, v[190:193]
	ds_write_b128 v137, v[190:193]
	ds_write_b128 v138, v[190:193]
	ds_write_b128 v139, v[190:193]
	ds_write_b128 v140, v[190:193]
	s_waitcnt lgkmcnt(6)
	global_store_dwordx4 v[158:159], v[162:165], off nt
	ds_write_b128 v141, v[190:193]
	s_waitcnt lgkmcnt(0)
	s_barrier
	s_cbranch_scc1 .LBB0_747
